# adds: expected-empty gathered tickets merged per list (walk on while non-empty); redundant barrier at the end of the conversion ticket removed
# baseline (speedup 1.0000x reference)
; #define GAS __attribute__((address_space(1)))
; #define LAS __attribute__((address_space(3)))
; __device__ __forceinline__ void cv8_out(const CvTile& cur, const LAS unsigned char* T, int tid_) {
;     const int nbl = cur.N / 256, kb = cur.r / nbl, nb = cur.r - kb * nbl;
; #pragma unroll
;     for (int i = 0; i < 4; ++i) { const int p = tid_ + 512 * i, c = p & 7, n = p >> 3, nn = 256 * nb + n;
;         const int drow = (cur.mode == 0) ? nn : (256 * (nn >> 7) + (nn & 127) + (cur.mode == 2 ? 128 : 0));
;         const v4u w = *(const LAS v4u*)(T + n * 128 + 16 * (c ^ ((n >> 2) & 7)));
;         __builtin_nontemporal_store(w, (GAS v4u*)(cur.WT + (size_t)drow * cur.K + 128 * kb + 16 * c)); }
.LBB0_494:
	s_waitcnt vmcnt(13)
	v_add_u32_e32 v10, s22, v101
	v_add_u32_e32 v2, v10, v99
	v_add_u32_e32 v3, v10, v96
	v_add_u32_e32 v4, v10, v92
	v_add_u32_e32 v5, v10, v89
	ds_read_b128 v[16:19], v2
	ds_read_b128 v[20:23], v3
	ds_read_b128 v[24:27], v4
	ds_read_b128 v[28:31], v5
	s_movk_i32 s3, 0x100
	s_movk_i32 s4, 0x140
	s_cmp_lg_u64 s[62:63], 0
	s_cselect_b32 s3, 0x80, s3
	s_cselect_b32 s4, 0xc0, s4
	v_add_u32_e32 v2, s64, v102
	v_lshlrev_b32_e32 v3, 1, v2
	v_and_b32_e32 v3, 0xffffff00, v3
	v_or3_b32 v3, v100, v3, s18
	v_cndmask_b32_e64 v8, v3, v2, s[62:63]
	v_ashrrev_i32_e32 v6, 31, v8
	v_mul_lo_u32 v11, s60, v6
	v_mov_b64_e32 v[6:7], s[58:59]
	v_mul_lo_u32 v12, s61, v8
	v_mad_u64_u32 v[8:9], s[0:1], s60, v8, v[6:7]
	s_ashr_i32 s71, s70, 31
	s_lshl_b64 s[42:43], s[60:61], 6
	s_mul_i32 s44, s60, s3
	s_mul_hi_u32 s45, s60, s3
	s_mul_i32 s54, s61, s3
	s_add_i32 s45, s45, s54
	s_mul_i32 s46, s60, s4
	s_mul_hi_u32 s47, s60, s4
	s_mul_i32 s54, s61, s4
	s_add_i32 s47, s47, s54
	v_add3_u32 v9, v12, v9, v11
	v_lshl_add_u64 v[8:9], v[8:9], 0, s[70:71]
	v_lshl_add_u64 v[8:9], v[8:9], 0, v[0:1]
	v_lshl_add_u64 v[32:33], v[8:9], 0, s[42:43]
	v_lshl_add_u64 v[34:35], v[8:9], 0, s[44:45]
	v_lshl_add_u64 v[36:37], v[8:9], 0, s[46:47]
	s_waitcnt lgkmcnt(3)
	global_store_dwordx4 v[8:9], v[16:19], off nt
	s_waitcnt lgkmcnt(2)
	global_store_dwordx4 v[32:33], v[20:23], off nt
	s_waitcnt lgkmcnt(1)
	global_store_dwordx4 v[34:35], v[24:27], off nt
	s_waitcnt lgkmcnt(0)
	global_store_dwordx4 v[36:37], v[28:31], off nt
	s_branch .LBB0_499
